# same stack without the MoE fifth-round split (its gain was within measurement noise): gathered-row batching, LDS gate table, carry-scan batching, early gate requests in the HGRN output pass, unrolled
# baseline (speedup 1.0000x reference)
.LBB0_1482:
	s_lshl_b32 s19, s0, 8
	s_and_b32 s19, s19, 0x300
	v_or_b32_e32 v187, s19, v183
	v_add_u32_e32 v152, v181, v1
	s_waitcnt vmcnt(0)
	v_and_b32_e32 v230, 0x80000001, v167
	v_cmp_eq_u32_e32 vcc, 0, v230
	s_and_saveexec_b64 s[38:39], vcc
	v_lshrrev_b32_e32 v230, 1, v167
	v_mov_b32_e32 v231, 0
	v_lshlrev_b64 v[230:231], 10, v[230:231]
	v_or_b32_e32 v230, v230, v187
	v_lshl_add_u64 v[230:231], v[230:231], 1, s[92:93]
	global_load_dwordx4 v[192:195], v[230:231], off
	global_load_dwordx4 v[196:199], v[230:231], off offset:256
	s_or_b64 exec, exec, s[38:39]
	v_and_b32_e32 v230, 0x80000001, v166
	v_cmp_eq_u32_e32 vcc, 0, v230
	s_and_saveexec_b64 s[38:39], vcc
	v_lshrrev_b32_e32 v230, 1, v166
	v_mov_b32_e32 v231, 0
	v_lshlrev_b64 v[230:231], 10, v[230:231]
	v_or_b32_e32 v230, v230, v187
	v_lshl_add_u64 v[230:231], v[230:231], 1, s[92:93]
	global_load_dwordx4 v[200:203], v[230:231], off
	global_load_dwordx4 v[204:207], v[230:231], off offset:256
	s_or_b64 exec, exec, s[38:39]
	v_and_b32_e32 v230, 0x80000001, v173
	v_cmp_eq_u32_e32 vcc, 0, v230
	s_and_saveexec_b64 s[38:39], vcc
	v_lshrrev_b32_e32 v230, 1, v173
	v_mov_b32_e32 v231, 0
	v_lshlrev_b64 v[230:231], 10, v[230:231]
	v_or_b32_e32 v230, v230, v187
	v_lshl_add_u64 v[230:231], v[230:231], 1, s[92:93]
	global_load_dwordx4 v[208:211], v[230:231], off
	global_load_dwordx4 v[212:215], v[230:231], off offset:256
	s_or_b64 exec, exec, s[38:39]
	v_and_b32_e32 v230, 0x80000001, v172
	v_cmp_eq_u32_e32 vcc, 0, v230
	s_and_saveexec_b64 s[38:39], vcc
	v_lshrrev_b32_e32 v230, 1, v172
	v_mov_b32_e32 v231, 0
	v_lshlrev_b64 v[230:231], 10, v[230:231]
	v_or_b32_e32 v230, v230, v187
	v_lshl_add_u64 v[230:231], v[230:231], 1, s[92:93]
	global_load_dwordx4 v[216:219], v[230:231], off
	global_load_dwordx4 v[220:223], v[230:231], off offset:256
	s_or_b64 exec, exec, s[38:39]
	v_and_b32_e32 v230, 0x80000001, v178
	v_cmp_eq_u32_e32 vcc, 0, v230
	s_and_saveexec_b64 s[38:39], vcc
	v_lshrrev_b32_e32 v230, 1, v178
	v_mov_b32_e32 v231, 0
	v_lshlrev_b64 v[230:231], 10, v[230:231]
	v_or_b32_e32 v230, v230, v187
	v_lshl_add_u64 v[230:231], v[230:231], 1, s[92:93]
	global_load_dwordx4 v[234:237], v[230:231], off
	global_load_dwordx4 v[238:241], v[230:231], off offset:256
	s_or_b64 exec, exec, s[38:39]
	v_and_b32_e32 v230, 0x80000001, v177
	v_cmp_eq_u32_e32 vcc, 0, v230
	s_and_saveexec_b64 s[38:39], vcc
	v_lshrrev_b32_e32 v230, 1, v177
	v_mov_b32_e32 v231, 0
	v_lshlrev_b64 v[230:231], 10, v[230:231]
	v_or_b32_e32 v230, v230, v187
	v_lshl_add_u64 v[230:231], v[230:231], 1, s[92:93]
	global_load_dwordx4 v[242:245], v[230:231], off
	global_load_dwordx4 v[246:249], v[230:231], off offset:256
	s_or_b64 exec, exec, s[38:39]
	v_cmp_lt_i32_e32 vcc, -1, v167
	v_ashrrev_i32_e32 v153, 31, v152
	v_lshlrev_b32_e32 v154, 2, v187
	v_add_u32_e32 v154, 0x21000, v154
	v_readlane_b32 s36, v253, 38
	v_readlane_b32 s37, v253, 39
	s_nop 1
	v_lshl_add_u64 v[156:157], v[152:153], 2, s[36:37]
	global_load_dword v158, v[156:157], off
	global_load_dword v189, v[156:157], off offset:64
	global_load_dword v190, v[156:157], off offset:128
	global_load_dword v191, v[156:157], off offset:192
	global_load_dword v250, v[156:157], off offset:640
	global_load_dword v155, v[156:157], off offset:704
	global_load_dword v152, v[156:157], off offset:512
	global_load_dword v153, v[156:157], off offset:576
	s_waitcnt vmcnt(0)
	s_and_saveexec_b64 s[34:35], vcc
	s_cbranch_execz .LBB0_1491
	v_lshrrev_b32_e32 v114, 14, v167
	v_lshl_add_u32 v160, v114, 12, v154
	ds_read_b128 v[132:135], v160
	ds_read_b128 v[136:139], v160 offset:16
	v_lshrrev_b32_e32 v156, 1, v167
	v_mov_b32_e32 v157, v115
	v_and_b32_e32 v114, 1, v167
	v_lshlrev_b64 v[156:157], 10, v[156:157]
	v_cmp_eq_u32_e32 vcc, 1, v114
	v_or_b32_e32 v162, v156, v187
	v_mov_b32_e32 v163, v157
	s_waitcnt lgkmcnt(1)
	v_pk_mul_f32 v[134:135], v[8:9], v[134:135]
	v_pk_mul_f32 v[132:133], v[6:7], v[132:133]
	s_waitcnt lgkmcnt(0)
	v_pk_mul_f32 v[138:139], v[130:131], v[138:139]
	v_pk_mul_f32 v[168:169], v[128:129], v[136:137]
	v_pk_mul_f32 v[164:165], v[158:159], v[134:135] op_sel_hi:[0,1]
	v_pk_mul_f32 v[136:137], v[158:159], v[132:133] op_sel_hi:[0,1]
	v_pk_mul_f32 v[138:139], v[158:159], v[138:139] op_sel_hi:[0,1]
	v_pk_mul_f32 v[132:133], v[158:159], v[168:169] op_sel_hi:[0,1]
	s_and_saveexec_b64 s[38:39], vcc
	s_xor_b64 s[38:39], exec, s[38:39]
	s_cbranch_execz .LBB0_1485
	v_cvt_pk_bf16_f32 v134, v136, v137
	v_cvt_pk_bf16_f32 v135, v164, v165
	v_cvt_pk_bf16_f32 v136, v132, v133
	v_cvt_pk_bf16_f32 v137, v138, v139
	v_lshl_add_u64 v[132:133], v[162:163], 1, s[4:5]
	global_store_dwordx4 v[132:133], v[134:137], off
